# select v4: histograms and threshold tests on raw float bits (key order restored in find_bin), no key conversion in pass 1/2/final
# speedup vs baseline: 1.0121x; 1.0043x over previous
.Lsel_p1_nold:
	s_cmp_le_i32 s36, s2
	s_cbranch_scc0 .Lsel_p1_tail
	v_bfe_u32 v34, v18, 21, 11
	v_lshl_add_u32 v34, v34, 2, s52
	ds_add_u32 v34, v57
	v_bfe_u32 v35, v19, 21, 11
	v_lshl_add_u32 v35, v35, 2, s52
	ds_add_u32 v35, v57
	v_bfe_u32 v36, v20, 21, 11
	v_lshl_add_u32 v36, v36, 2, s52
	ds_add_u32 v36, v57
	v_bfe_u32 v37, v21, 21, 11
	v_lshl_add_u32 v37, v37, 2, s52
	ds_add_u32 v37, v57
	v_bfe_u32 v38, v22, 21, 11
	v_lshl_add_u32 v38, v38, 2, s52
	ds_add_u32 v38, v57
	v_bfe_u32 v39, v23, 21, 11
	v_lshl_add_u32 v39, v39, 2, s52
	ds_add_u32 v39, v57
	v_bfe_u32 v40, v24, 21, 11
	v_lshl_add_u32 v40, v40, 2, s52
	ds_add_u32 v40, v57
	v_bfe_u32 v41, v25, 21, 11
	v_lshl_add_u32 v41, v41, 2, s52
	ds_add_u32 v41, v57
	v_bfe_u32 v42, v26, 21, 11
	v_lshl_add_u32 v42, v42, 2, s52
	ds_add_u32 v42, v57
	v_bfe_u32 v43, v27, 21, 11
	v_lshl_add_u32 v43, v43, 2, s52
	ds_add_u32 v43, v57
	v_bfe_u32 v44, v28, 21, 11
	v_lshl_add_u32 v44, v44, 2, s52
	ds_add_u32 v44, v57
	v_bfe_u32 v45, v29, 21, 11
	v_lshl_add_u32 v45, v45, 2, s52
	ds_add_u32 v45, v57
	v_bfe_u32 v46, v30, 21, 11
	v_lshl_add_u32 v46, v46, 2, s52
	ds_add_u32 v46, v57
	v_bfe_u32 v47, v31, 21, 11
	v_lshl_add_u32 v47, v47, 2, s52
	ds_add_u32 v47, v57
	v_bfe_u32 v48, v32, 21, 11
	v_lshl_add_u32 v48, v48, 2, s52
	ds_add_u32 v48, v57
	v_bfe_u32 v49, v33, 21, 11
	v_lshl_add_u32 v49, v49, 2, s52
	ds_add_u32 v49, v57
	s_mov_b32 s16, s36
	s_cmp_lt_i32 s16, s2
	s_cbranch_scc0 .Lsel_p1_done
	s_waitcnt vmcnt(0)
	s_branch .Lsel_p1_loop
.Lsel_p1_tail:
	s_sub_i32 s37, s2, s16
	v_sub_u32_e32 v134, s37, v56
	v_cmpx_lt_i32_e32 vcc, 0, v134
	v_bfe_u32 v34, v18, 21, 11
	v_lshl_add_u32 v34, v34, 2, s52
	ds_add_u32 v34, v57
	v_cmpx_lt_i32_e32 vcc, 1, v134
	v_bfe_u32 v35, v19, 21, 11
	v_lshl_add_u32 v35, v35, 2, s52
	ds_add_u32 v35, v57
	v_cmpx_lt_i32_e32 vcc, 2, v134
	v_bfe_u32 v36, v20, 21, 11
	v_lshl_add_u32 v36, v36, 2, s52
	ds_add_u32 v36, v57
	v_cmpx_lt_i32_e32 vcc, 3, v134
	v_bfe_u32 v37, v21, 21, 11
	v_lshl_add_u32 v37, v37, 2, s52
	ds_add_u32 v37, v57
	v_cmpx_lt_i32_e32 vcc, 0x100, v134
	v_bfe_u32 v38, v22, 21, 11
	v_lshl_add_u32 v38, v38, 2, s52
	ds_add_u32 v38, v57
	v_cmpx_lt_i32_e32 vcc, 0x101, v134
	v_bfe_u32 v39, v23, 21, 11
	v_lshl_add_u32 v39, v39, 2, s52
	ds_add_u32 v39, v57
	v_cmpx_lt_i32_e32 vcc, 0x102, v134
	v_bfe_u32 v40, v24, 21, 11
	v_lshl_add_u32 v40, v40, 2, s52
	ds_add_u32 v40, v57
	v_cmpx_lt_i32_e32 vcc, 0x103, v134
	v_bfe_u32 v41, v25, 21, 11
	v_lshl_add_u32 v41, v41, 2, s52
	ds_add_u32 v41, v57
	v_cmpx_lt_i32_e32 vcc, 0x200, v134
	v_bfe_u32 v42, v26, 21, 11
	v_lshl_add_u32 v42, v42, 2, s52
	ds_add_u32 v42, v57
	v_cmpx_lt_i32_e32 vcc, 0x201, v134
	v_bfe_u32 v43, v27, 21, 11
	v_lshl_add_u32 v43, v43, 2, s52
	ds_add_u32 v43, v57
	v_cmpx_lt_i32_e32 vcc, 0x202, v134
	v_bfe_u32 v44, v28, 21, 11
	v_lshl_add_u32 v44, v44, 2, s52
	ds_add_u32 v44, v57
	v_cmpx_lt_i32_e32 vcc, 0x203, v134
	v_bfe_u32 v45, v29, 21, 11
	v_lshl_add_u32 v45, v45, 2, s52
	ds_add_u32 v45, v57
	v_cmpx_lt_i32_e32 vcc, 0x300, v134
	v_bfe_u32 v46, v30, 21, 11
	v_lshl_add_u32 v46, v46, 2, s52
	ds_add_u32 v46, v57
	v_cmpx_lt_i32_e32 vcc, 0x301, v134
	v_bfe_u32 v47, v31, 21, 11
	v_lshl_add_u32 v47, v47, 2, s52
	ds_add_u32 v47, v57
	v_cmpx_lt_i32_e32 vcc, 0x302, v134
	v_bfe_u32 v48, v32, 21, 11
	v_lshl_add_u32 v48, v48, 2, s52
	ds_add_u32 v48, v57
	v_cmpx_lt_i32_e32 vcc, 0x303, v134
	v_bfe_u32 v49, v33, 21, 11
	v_lshl_add_u32 v49, v49, 2, s52
	ds_add_u32 v49, v57
	s_mov_b64 exec, -1
.Lsel_p1_done:
	s_waitcnt lgkmcnt(0)
	v_lshlrev_b32_e32 v34, 7, v50
	v_sub_u32_e32 v44, 0x1f80, v34
	v_add_u32_e32 v34, 0xfffff000, v34
	v_cmp_gt_u32_e32 vcc, 32, v50
	s_nop 1
	v_cndmask_b32_e32 v34, v34, v44, vcc
	v_add_u32_e32 v34, s52, v34
	ds_read_b128 v[2:5], v34
	ds_read_b128 v[6:9], v34 offset:16
	ds_read_b128 v[10:13], v34 offset:32
	ds_read_b128 v[14:17], v34 offset:48
	ds_read_b128 v[18:21], v34 offset:64
	ds_read_b128 v[22:25], v34 offset:80
	ds_read_b128 v[26:29], v34 offset:96
	ds_read_b128 v[30:33], v34 offset:112
	s_waitcnt lgkmcnt(0)
	v_add_u32_e32 v35, v2, v3
	v_add3_u32 v35, v35, v4, v5
	v_add3_u32 v35, v35, v6, v7
	v_add3_u32 v35, v35, v8, v9
	v_add3_u32 v35, v35, v10, v11
	v_add3_u32 v35, v35, v12, v13
	v_add3_u32 v35, v35, v14, v15
	v_add3_u32 v35, v35, v16, v17
	v_add3_u32 v35, v35, v18, v19
	v_add3_u32 v35, v35, v20, v21
	v_add3_u32 v35, v35, v22, v23
	v_add3_u32 v35, v35, v24, v25
	v_add3_u32 v35, v35, v26, v27
	v_add3_u32 v35, v35, v28, v29
	v_add3_u32 v35, v35, v30, v31
	v_add3_u32 v35, v35, v32, v33
	v_mov_b32_e32 v36, v35
	s_nop 1
	v_add_u32_dpp v36, v36, v36 row_shr:1 row_mask:0xf bank_mask:0xf bound_ctrl:1
	s_nop 1
	v_add_u32_dpp v36, v36, v36 row_shr:2 row_mask:0xf bank_mask:0xf bound_ctrl:1
	s_nop 1
	v_add_u32_dpp v36, v36, v36 row_shr:4 row_mask:0xf bank_mask:0xf bound_ctrl:1
	s_nop 1
	v_add_u32_dpp v36, v36, v36 row_shr:8 row_mask:0xf bank_mask:0xf bound_ctrl:1
	s_nop 1
	v_add_u32_dpp v36, v36, v36 row_bcast:15 row_mask:0xa bank_mask:0xf
	s_nop 1
	v_add_u32_dpp v36, v36, v36 row_bcast:31 row_mask:0xc bank_mask:0xf
	s_nop 0
	v_readlane_b32 s4, v36, 63
	s_nop 1
	v_sub_u32_e32 v37, s4, v36
	v_add_u32_e32 v38, v37, v35
	v_cmp_gt_u32_e32 vcc, s15, v37
	v_cmp_le_u32_e64 s[4:5], s15, v38
	s_and_b64 s[4:5], vcc, s[4:5]
	s_ff1_i32_b64 s6, s[4:5]
	v_readlane_b32 s7, v37, s6
	s_lshl_b32 s10, s6, 7
	s_sub_i32 s11, 0x1f80, s10
	s_add_i32 s10, s10, 0xfffff07c
	s_cmp_ge_u32 s6, 32
	s_cselect_b32 s10, s10, s11
	s_cselect_b32 s34, -1, 1
	s_add_i32 s10, s10, s52
	v_and_b32_e32 v39, 31, v50
	v_lshlrev_b32_e32 v39, 2, v39
	v_mul_i32_i24_e32 v39, s34, v39
	v_add_u32_e32 v39, s10, v39
	ds_read_b32 v40, v39
	v_cmp_gt_u32_e32 vcc, 32, v50
	s_waitcnt lgkmcnt(0)
	s_nop 1
	v_cndmask_b32_e32 v40, 0, v40, vcc
	v_mov_b32_e32 v41, v40
	s_nop 1
	v_add_u32_dpp v41, v41, v41 row_shr:1 row_mask:0xf bank_mask:0xf bound_ctrl:1
	s_nop 1
	v_add_u32_dpp v41, v41, v41 row_shr:2 row_mask:0xf bank_mask:0xf bound_ctrl:1
	s_nop 1
	v_add_u32_dpp v41, v41, v41 row_shr:4 row_mask:0xf bank_mask:0xf bound_ctrl:1
	s_nop 1
	v_add_u32_dpp v41, v41, v41 row_shr:8 row_mask:0xf bank_mask:0xf bound_ctrl:1
	s_nop 1
	v_add_u32_dpp v41, v41, v41 row_bcast:15 row_mask:0xa bank_mask:0xf
	s_nop 1
	v_add_u32_dpp v41, v41, v41 row_bcast:31 row_mask:0xc bank_mask:0xf
	s_nop 0
	v_sub_u32_e32 v42, v41, v40
	v_add_u32_e32 v42, s7, v42
	v_add_u32_e32 v43, v42, v40
	v_cmp_gt_u32_e32 vcc, s15, v42
	v_cmp_le_u32_e64 s[4:5], s15, v43
	s_and_b64 s[4:5], vcc, s[4:5]
	s_ff1_i32_b64 s11, s[4:5]
	v_readlane_b32 s14, v40, s11
	v_readlane_b32 s5, v42, s11
	s_lshl_b32 s30, s6, 5
	s_sub_i32 s4, 31, s11
	s_add_i32 s30, s30, s4
	s_sub_i32 s15, s15, s5
	s_cmp_lt_u32 s30, 0x400
	s_cselect_b32 s31, 1, 0
	s_add_i32 s4, s30, 0xfffffc00
	s_sub_i32 s5, 0x7ff, s30
	s_cmp_lg_u32 s31, 0
	s_cselect_b32 s13, s5, s4
	s_mov_b64 s[8:9], s[42:43]
	global_load_dwordx4 v[2:5], v58, s[8:9]
	global_load_dwordx4 v[6:9], v58, s[8:9] offset:1024
	global_load_dwordx4 v[10:13], v58, s[8:9] offset:2048
	global_load_dwordx4 v[14:17], v58, s[8:9] offset:3072
	ds_write_b128 v64, v[150:153]
	ds_write_b128 v64, v[150:153] offset:1024
	ds_write_b128 v64, v[150:153] offset:2048
	ds_write_b128 v64, v[150:153] offset:3072
	ds_write_b128 v64, v[150:153] offset:4096
	ds_write_b128 v64, v[150:153] offset:5120
	ds_write_b128 v64, v[150:153] offset:6144
	ds_write_b128 v64, v[150:153] offset:7168
	s_cmpk_le_u32 s14, 0x800
	s_cselect_b32 s25, -1, 0
	s_add_i32 s24, s52, 0x2000
	s_mov_b32 s16, 0
	s_waitcnt vmcnt(0)

.Lsel_p2_nold:
	s_cmp_le_i32 s36, s2
	s_cbranch_scc0 .Lsel_p2_tail
	v_lshrrev_b32_e32 v118, 21, v18
	v_lshrrev_b32_e32 v119, 21, v19
	v_lshrrev_b32_e32 v120, 21, v20
	v_lshrrev_b32_e32 v121, 21, v21
	v_lshrrev_b32_e32 v122, 21, v22
	v_lshrrev_b32_e32 v123, 21, v23
	v_lshrrev_b32_e32 v124, 21, v24
	v_lshrrev_b32_e32 v125, 21, v25
	v_lshrrev_b32_e32 v126, 21, v26
	v_lshrrev_b32_e32 v127, 21, v27
	v_lshrrev_b32_e32 v128, 21, v28
	v_lshrrev_b32_e32 v129, 21, v29
	v_lshrrev_b32_e32 v130, 21, v30
	v_lshrrev_b32_e32 v131, 21, v31
	v_lshrrev_b32_e32 v132, 21, v32
	v_lshrrev_b32_e32 v133, 21, v33
	v_cmpx_eq_u32_e32 vcc, s13, v118
	v_bfe_u32 v118, v18, 10, 11
	v_lshl_add_u32 v118, v118, 2, s52
	ds_add_u32 v118, v57
	v_mbcnt_lo_u32_b32 v118, vcc_lo, 0
	v_mbcnt_hi_u32_b32 v118, vcc_hi, v118
	v_lshl_add_u32 v118, v118, 2, s24
	ds_write_b32 v118, v18
	s_bcnt1_i32_b64 s5, vcc
	s_and_b32 s5, s5, s25
	s_lshl2_add_u32 s24, s5, s24
	s_mov_b64 exec, -1
	v_cmpx_eq_u32_e32 vcc, s13, v119
	v_bfe_u32 v119, v19, 10, 11
	v_lshl_add_u32 v119, v119, 2, s52
	ds_add_u32 v119, v57
	v_mbcnt_lo_u32_b32 v119, vcc_lo, 0
	v_mbcnt_hi_u32_b32 v119, vcc_hi, v119
	v_lshl_add_u32 v119, v119, 2, s24
	ds_write_b32 v119, v19
	s_bcnt1_i32_b64 s5, vcc
	s_and_b32 s5, s5, s25
	s_lshl2_add_u32 s24, s5, s24
	s_mov_b64 exec, -1
	v_cmpx_eq_u32_e32 vcc, s13, v120
	v_bfe_u32 v120, v20, 10, 11
	v_lshl_add_u32 v120, v120, 2, s52
	ds_add_u32 v120, v57
	v_mbcnt_lo_u32_b32 v120, vcc_lo, 0
	v_mbcnt_hi_u32_b32 v120, vcc_hi, v120
	v_lshl_add_u32 v120, v120, 2, s24
	ds_write_b32 v120, v20
	s_bcnt1_i32_b64 s5, vcc
	s_and_b32 s5, s5, s25
	s_lshl2_add_u32 s24, s5, s24
	s_mov_b64 exec, -1
	v_cmpx_eq_u32_e32 vcc, s13, v121
	v_bfe_u32 v121, v21, 10, 11
	v_lshl_add_u32 v121, v121, 2, s52
	ds_add_u32 v121, v57
	v_mbcnt_lo_u32_b32 v121, vcc_lo, 0
	v_mbcnt_hi_u32_b32 v121, vcc_hi, v121
	v_lshl_add_u32 v121, v121, 2, s24
	ds_write_b32 v121, v21
	s_bcnt1_i32_b64 s5, vcc
	s_and_b32 s5, s5, s25
	s_lshl2_add_u32 s24, s5, s24
	s_mov_b64 exec, -1
	v_cmpx_eq_u32_e32 vcc, s13, v122
	v_bfe_u32 v122, v22, 10, 11
	v_lshl_add_u32 v122, v122, 2, s52
	ds_add_u32 v122, v57
	v_mbcnt_lo_u32_b32 v122, vcc_lo, 0
	v_mbcnt_hi_u32_b32 v122, vcc_hi, v122
	v_lshl_add_u32 v122, v122, 2, s24
	ds_write_b32 v122, v22
	s_bcnt1_i32_b64 s5, vcc
	s_and_b32 s5, s5, s25
	s_lshl2_add_u32 s24, s5, s24
	s_mov_b64 exec, -1
	v_cmpx_eq_u32_e32 vcc, s13, v123
	v_bfe_u32 v123, v23, 10, 11
	v_lshl_add_u32 v123, v123, 2, s52
	ds_add_u32 v123, v57
	v_mbcnt_lo_u32_b32 v123, vcc_lo, 0
	v_mbcnt_hi_u32_b32 v123, vcc_hi, v123
	v_lshl_add_u32 v123, v123, 2, s24
	ds_write_b32 v123, v23
	s_bcnt1_i32_b64 s5, vcc
	s_and_b32 s5, s5, s25
	s_lshl2_add_u32 s24, s5, s24
	s_mov_b64 exec, -1
	v_cmpx_eq_u32_e32 vcc, s13, v124
	v_bfe_u32 v124, v24, 10, 11
	v_lshl_add_u32 v124, v124, 2, s52
	ds_add_u32 v124, v57
	v_mbcnt_lo_u32_b32 v124, vcc_lo, 0
	v_mbcnt_hi_u32_b32 v124, vcc_hi, v124
	v_lshl_add_u32 v124, v124, 2, s24
	ds_write_b32 v124, v24
	s_bcnt1_i32_b64 s5, vcc
	s_and_b32 s5, s5, s25
	s_lshl2_add_u32 s24, s5, s24
	s_mov_b64 exec, -1
	v_cmpx_eq_u32_e32 vcc, s13, v125
	v_bfe_u32 v125, v25, 10, 11
	v_lshl_add_u32 v125, v125, 2, s52
	ds_add_u32 v125, v57
	v_mbcnt_lo_u32_b32 v125, vcc_lo, 0
	v_mbcnt_hi_u32_b32 v125, vcc_hi, v125
	v_lshl_add_u32 v125, v125, 2, s24
	ds_write_b32 v125, v25
	s_bcnt1_i32_b64 s5, vcc
	s_and_b32 s5, s5, s25
	s_lshl2_add_u32 s24, s5, s24
	s_mov_b64 exec, -1
	v_cmpx_eq_u32_e32 vcc, s13, v126
	v_bfe_u32 v126, v26, 10, 11
	v_lshl_add_u32 v126, v126, 2, s52
	ds_add_u32 v126, v57
	v_mbcnt_lo_u32_b32 v126, vcc_lo, 0
	v_mbcnt_hi_u32_b32 v126, vcc_hi, v126
	v_lshl_add_u32 v126, v126, 2, s24
	ds_write_b32 v126, v26
	s_bcnt1_i32_b64 s5, vcc
	s_and_b32 s5, s5, s25
	s_lshl2_add_u32 s24, s5, s24
	s_mov_b64 exec, -1
	v_cmpx_eq_u32_e32 vcc, s13, v127
	v_bfe_u32 v127, v27, 10, 11
	v_lshl_add_u32 v127, v127, 2, s52
	ds_add_u32 v127, v57
	v_mbcnt_lo_u32_b32 v127, vcc_lo, 0
	v_mbcnt_hi_u32_b32 v127, vcc_hi, v127
	v_lshl_add_u32 v127, v127, 2, s24
	ds_write_b32 v127, v27
	s_bcnt1_i32_b64 s5, vcc
	s_and_b32 s5, s5, s25
	s_lshl2_add_u32 s24, s5, s24
	s_mov_b64 exec, -1
	v_cmpx_eq_u32_e32 vcc, s13, v128
	v_bfe_u32 v128, v28, 10, 11
	v_lshl_add_u32 v128, v128, 2, s52
	ds_add_u32 v128, v57
	v_mbcnt_lo_u32_b32 v128, vcc_lo, 0
	v_mbcnt_hi_u32_b32 v128, vcc_hi, v128
	v_lshl_add_u32 v128, v128, 2, s24
	ds_write_b32 v128, v28
	s_bcnt1_i32_b64 s5, vcc
	s_and_b32 s5, s5, s25
	s_lshl2_add_u32 s24, s5, s24
	s_mov_b64 exec, -1
	v_cmpx_eq_u32_e32 vcc, s13, v129
	v_bfe_u32 v129, v29, 10, 11
	v_lshl_add_u32 v129, v129, 2, s52
	ds_add_u32 v129, v57
	v_mbcnt_lo_u32_b32 v129, vcc_lo, 0
	v_mbcnt_hi_u32_b32 v129, vcc_hi, v129
	v_lshl_add_u32 v129, v129, 2, s24
	ds_write_b32 v129, v29
	s_bcnt1_i32_b64 s5, vcc
	s_and_b32 s5, s5, s25
	s_lshl2_add_u32 s24, s5, s24
	s_mov_b64 exec, -1
	v_cmpx_eq_u32_e32 vcc, s13, v130
	v_bfe_u32 v130, v30, 10, 11
	v_lshl_add_u32 v130, v130, 2, s52
	ds_add_u32 v130, v57
	v_mbcnt_lo_u32_b32 v130, vcc_lo, 0
	v_mbcnt_hi_u32_b32 v130, vcc_hi, v130
	v_lshl_add_u32 v130, v130, 2, s24
	ds_write_b32 v130, v30
	s_bcnt1_i32_b64 s5, vcc
	s_and_b32 s5, s5, s25
	s_lshl2_add_u32 s24, s5, s24
	s_mov_b64 exec, -1
	v_cmpx_eq_u32_e32 vcc, s13, v131
	v_bfe_u32 v131, v31, 10, 11
	v_lshl_add_u32 v131, v131, 2, s52
	ds_add_u32 v131, v57
	v_mbcnt_lo_u32_b32 v131, vcc_lo, 0
	v_mbcnt_hi_u32_b32 v131, vcc_hi, v131
	v_lshl_add_u32 v131, v131, 2, s24
	ds_write_b32 v131, v31
	s_bcnt1_i32_b64 s5, vcc
	s_and_b32 s5, s5, s25
	s_lshl2_add_u32 s24, s5, s24
	s_mov_b64 exec, -1
	v_cmpx_eq_u32_e32 vcc, s13, v132
	v_bfe_u32 v132, v32, 10, 11
	v_lshl_add_u32 v132, v132, 2, s52
	ds_add_u32 v132, v57
	v_mbcnt_lo_u32_b32 v132, vcc_lo, 0
	v_mbcnt_hi_u32_b32 v132, vcc_hi, v132
	v_lshl_add_u32 v132, v132, 2, s24
	ds_write_b32 v132, v32
	s_bcnt1_i32_b64 s5, vcc
	s_and_b32 s5, s5, s25
	s_lshl2_add_u32 s24, s5, s24
	s_mov_b64 exec, -1
	v_cmpx_eq_u32_e32 vcc, s13, v133
	v_bfe_u32 v133, v33, 10, 11
	v_lshl_add_u32 v133, v133, 2, s52
	ds_add_u32 v133, v57
	v_mbcnt_lo_u32_b32 v133, vcc_lo, 0
	v_mbcnt_hi_u32_b32 v133, vcc_hi, v133
	v_lshl_add_u32 v133, v133, 2, s24
	ds_write_b32 v133, v33
	s_bcnt1_i32_b64 s5, vcc
	s_and_b32 s5, s5, s25
	s_lshl2_add_u32 s24, s5, s24
	s_mov_b64 exec, -1
	s_mov_b32 s16, s36
	s_cmp_lt_i32 s16, s2
	s_cbranch_scc0 .Lsel_p2_done
	s_waitcnt vmcnt(0)
	s_branch .Lsel_p2_loop
.Lsel_p2_tail:
	s_sub_i32 s37, s2, s16
	v_sub_u32_e32 v134, s37, v56
	v_lshrrev_b32_e32 v118, 21, v18
	v_lshrrev_b32_e32 v119, 21, v19
	v_lshrrev_b32_e32 v120, 21, v20
	v_lshrrev_b32_e32 v121, 21, v21
	v_lshrrev_b32_e32 v122, 21, v22
	v_lshrrev_b32_e32 v123, 21, v23
	v_lshrrev_b32_e32 v124, 21, v24
	v_lshrrev_b32_e32 v125, 21, v25
	v_lshrrev_b32_e32 v126, 21, v26
	v_lshrrev_b32_e32 v127, 21, v27
	v_lshrrev_b32_e32 v128, 21, v28
	v_lshrrev_b32_e32 v129, 21, v29
	v_lshrrev_b32_e32 v130, 21, v30
	v_lshrrev_b32_e32 v131, 21, v31
	v_lshrrev_b32_e32 v132, 21, v32
	v_lshrrev_b32_e32 v133, 21, v33
	v_cmpx_lt_i32_e32 vcc, 0, v134
	v_cmpx_eq_u32_e32 vcc, s13, v118
	v_bfe_u32 v118, v18, 10, 11
	v_lshl_add_u32 v118, v118, 2, s52
	ds_add_u32 v118, v57
	v_mbcnt_lo_u32_b32 v118, vcc_lo, 0
	v_mbcnt_hi_u32_b32 v118, vcc_hi, v118
	v_lshl_add_u32 v118, v118, 2, s24
	ds_write_b32 v118, v18
	s_bcnt1_i32_b64 s5, vcc
	s_and_b32 s5, s5, s25
	s_lshl2_add_u32 s24, s5, s24
	s_mov_b64 exec, -1
	v_cmpx_lt_i32_e32 vcc, 1, v134
	v_cmpx_eq_u32_e32 vcc, s13, v119
	v_bfe_u32 v119, v19, 10, 11
	v_lshl_add_u32 v119, v119, 2, s52
	ds_add_u32 v119, v57
	v_mbcnt_lo_u32_b32 v119, vcc_lo, 0
	v_mbcnt_hi_u32_b32 v119, vcc_hi, v119
	v_lshl_add_u32 v119, v119, 2, s24
	ds_write_b32 v119, v19
	s_bcnt1_i32_b64 s5, vcc
	s_and_b32 s5, s5, s25
	s_lshl2_add_u32 s24, s5, s24
	s_mov_b64 exec, -1
	v_cmpx_lt_i32_e32 vcc, 2, v134
	v_cmpx_eq_u32_e32 vcc, s13, v120
	v_bfe_u32 v120, v20, 10, 11
	v_lshl_add_u32 v120, v120, 2, s52
	ds_add_u32 v120, v57
	v_mbcnt_lo_u32_b32 v120, vcc_lo, 0
	v_mbcnt_hi_u32_b32 v120, vcc_hi, v120
	v_lshl_add_u32 v120, v120, 2, s24
	ds_write_b32 v120, v20
	s_bcnt1_i32_b64 s5, vcc
	s_and_b32 s5, s5, s25
	s_lshl2_add_u32 s24, s5, s24
	s_mov_b64 exec, -1
	v_cmpx_lt_i32_e32 vcc, 3, v134
	v_cmpx_eq_u32_e32 vcc, s13, v121
	v_bfe_u32 v121, v21, 10, 11
	v_lshl_add_u32 v121, v121, 2, s52
	ds_add_u32 v121, v57
	v_mbcnt_lo_u32_b32 v121, vcc_lo, 0
	v_mbcnt_hi_u32_b32 v121, vcc_hi, v121
	v_lshl_add_u32 v121, v121, 2, s24
	ds_write_b32 v121, v21
	s_bcnt1_i32_b64 s5, vcc
	s_and_b32 s5, s5, s25
	s_lshl2_add_u32 s24, s5, s24
	s_mov_b64 exec, -1
	v_cmpx_lt_i32_e32 vcc, 0x100, v134
	v_cmpx_eq_u32_e32 vcc, s13, v122
	v_bfe_u32 v122, v22, 10, 11
	v_lshl_add_u32 v122, v122, 2, s52
	ds_add_u32 v122, v57
	v_mbcnt_lo_u32_b32 v122, vcc_lo, 0
	v_mbcnt_hi_u32_b32 v122, vcc_hi, v122
	v_lshl_add_u32 v122, v122, 2, s24
	ds_write_b32 v122, v22
	s_bcnt1_i32_b64 s5, vcc
	s_and_b32 s5, s5, s25
	s_lshl2_add_u32 s24, s5, s24
	s_mov_b64 exec, -1
	v_cmpx_lt_i32_e32 vcc, 0x101, v134
	v_cmpx_eq_u32_e32 vcc, s13, v123
	v_bfe_u32 v123, v23, 10, 11
	v_lshl_add_u32 v123, v123, 2, s52
	ds_add_u32 v123, v57
	v_mbcnt_lo_u32_b32 v123, vcc_lo, 0
	v_mbcnt_hi_u32_b32 v123, vcc_hi, v123
	v_lshl_add_u32 v123, v123, 2, s24
	ds_write_b32 v123, v23
	s_bcnt1_i32_b64 s5, vcc
	s_and_b32 s5, s5, s25
	s_lshl2_add_u32 s24, s5, s24
	s_mov_b64 exec, -1
	v_cmpx_lt_i32_e32 vcc, 0x102, v134
	v_cmpx_eq_u32_e32 vcc, s13, v124
	v_bfe_u32 v124, v24, 10, 11
	v_lshl_add_u32 v124, v124, 2, s52
	ds_add_u32 v124, v57
	v_mbcnt_lo_u32_b32 v124, vcc_lo, 0
	v_mbcnt_hi_u32_b32 v124, vcc_hi, v124
	v_lshl_add_u32 v124, v124, 2, s24
	ds_write_b32 v124, v24
	s_bcnt1_i32_b64 s5, vcc
	s_and_b32 s5, s5, s25
	s_lshl2_add_u32 s24, s5, s24
	s_mov_b64 exec, -1
	v_cmpx_lt_i32_e32 vcc, 0x103, v134
	v_cmpx_eq_u32_e32 vcc, s13, v125
	v_bfe_u32 v125, v25, 10, 11
	v_lshl_add_u32 v125, v125, 2, s52
	ds_add_u32 v125, v57
	v_mbcnt_lo_u32_b32 v125, vcc_lo, 0
	v_mbcnt_hi_u32_b32 v125, vcc_hi, v125
	v_lshl_add_u32 v125, v125, 2, s24
	ds_write_b32 v125, v25
	s_bcnt1_i32_b64 s5, vcc
	s_and_b32 s5, s5, s25
	s_lshl2_add_u32 s24, s5, s24
	s_mov_b64 exec, -1
	v_cmpx_lt_i32_e32 vcc, 0x200, v134
	v_cmpx_eq_u32_e32 vcc, s13, v126
	v_bfe_u32 v126, v26, 10, 11
	v_lshl_add_u32 v126, v126, 2, s52
	ds_add_u32 v126, v57
	v_mbcnt_lo_u32_b32 v126, vcc_lo, 0
	v_mbcnt_hi_u32_b32 v126, vcc_hi, v126
	v_lshl_add_u32 v126, v126, 2, s24
	ds_write_b32 v126, v26
	s_bcnt1_i32_b64 s5, vcc
	s_and_b32 s5, s5, s25
	s_lshl2_add_u32 s24, s5, s24
	s_mov_b64 exec, -1
	v_cmpx_lt_i32_e32 vcc, 0x201, v134
	v_cmpx_eq_u32_e32 vcc, s13, v127
	v_bfe_u32 v127, v27, 10, 11
	v_lshl_add_u32 v127, v127, 2, s52
	ds_add_u32 v127, v57
	v_mbcnt_lo_u32_b32 v127, vcc_lo, 0
	v_mbcnt_hi_u32_b32 v127, vcc_hi, v127
	v_lshl_add_u32 v127, v127, 2, s24
	ds_write_b32 v127, v27
	s_bcnt1_i32_b64 s5, vcc
	s_and_b32 s5, s5, s25
	s_lshl2_add_u32 s24, s5, s24
	s_mov_b64 exec, -1
	v_cmpx_lt_i32_e32 vcc, 0x202, v134
	v_cmpx_eq_u32_e32 vcc, s13, v128
	v_bfe_u32 v128, v28, 10, 11
	v_lshl_add_u32 v128, v128, 2, s52
	ds_add_u32 v128, v57
	v_mbcnt_lo_u32_b32 v128, vcc_lo, 0
	v_mbcnt_hi_u32_b32 v128, vcc_hi, v128
	v_lshl_add_u32 v128, v128, 2, s24
	ds_write_b32 v128, v28
	s_bcnt1_i32_b64 s5, vcc
	s_and_b32 s5, s5, s25
	s_lshl2_add_u32 s24, s5, s24
	s_mov_b64 exec, -1
	v_cmpx_lt_i32_e32 vcc, 0x203, v134
	v_cmpx_eq_u32_e32 vcc, s13, v129
	v_bfe_u32 v129, v29, 10, 11
	v_lshl_add_u32 v129, v129, 2, s52
	ds_add_u32 v129, v57
	v_mbcnt_lo_u32_b32 v129, vcc_lo, 0
	v_mbcnt_hi_u32_b32 v129, vcc_hi, v129
	v_lshl_add_u32 v129, v129, 2, s24
	ds_write_b32 v129, v29
	s_bcnt1_i32_b64 s5, vcc
	s_and_b32 s5, s5, s25
	s_lshl2_add_u32 s24, s5, s24
	s_mov_b64 exec, -1
	v_cmpx_lt_i32_e32 vcc, 0x300, v134
	v_cmpx_eq_u32_e32 vcc, s13, v130
	v_bfe_u32 v130, v30, 10, 11
	v_lshl_add_u32 v130, v130, 2, s52
	ds_add_u32 v130, v57
	v_mbcnt_lo_u32_b32 v130, vcc_lo, 0
	v_mbcnt_hi_u32_b32 v130, vcc_hi, v130
	v_lshl_add_u32 v130, v130, 2, s24
	ds_write_b32 v130, v30
	s_bcnt1_i32_b64 s5, vcc
	s_and_b32 s5, s5, s25
	s_lshl2_add_u32 s24, s5, s24
	s_mov_b64 exec, -1
	v_cmpx_lt_i32_e32 vcc, 0x301, v134
	v_cmpx_eq_u32_e32 vcc, s13, v131
	v_bfe_u32 v131, v31, 10, 11
	v_lshl_add_u32 v131, v131, 2, s52
	ds_add_u32 v131, v57
	v_mbcnt_lo_u32_b32 v131, vcc_lo, 0
	v_mbcnt_hi_u32_b32 v131, vcc_hi, v131
	v_lshl_add_u32 v131, v131, 2, s24
	ds_write_b32 v131, v31
	s_bcnt1_i32_b64 s5, vcc
	s_and_b32 s5, s5, s25
	s_lshl2_add_u32 s24, s5, s24
	s_mov_b64 exec, -1
	v_cmpx_lt_i32_e32 vcc, 0x302, v134
	v_cmpx_eq_u32_e32 vcc, s13, v132
	v_bfe_u32 v132, v32, 10, 11
	v_lshl_add_u32 v132, v132, 2, s52
	ds_add_u32 v132, v57
	v_mbcnt_lo_u32_b32 v132, vcc_lo, 0
	v_mbcnt_hi_u32_b32 v132, vcc_hi, v132
	v_lshl_add_u32 v132, v132, 2, s24
	ds_write_b32 v132, v32
	s_bcnt1_i32_b64 s5, vcc
	s_and_b32 s5, s5, s25
	s_lshl2_add_u32 s24, s5, s24
	s_mov_b64 exec, -1
	v_cmpx_lt_i32_e32 vcc, 0x303, v134
	v_cmpx_eq_u32_e32 vcc, s13, v133
	v_bfe_u32 v133, v33, 10, 11
	v_lshl_add_u32 v133, v133, 2, s52
	ds_add_u32 v133, v57
	v_mbcnt_lo_u32_b32 v133, vcc_lo, 0
	v_mbcnt_hi_u32_b32 v133, vcc_hi, v133
	v_lshl_add_u32 v133, v133, 2, s24
	ds_write_b32 v133, v33
	s_bcnt1_i32_b64 s5, vcc
	s_and_b32 s5, s5, s25
	s_lshl2_add_u32 s24, s5, s24
	s_mov_b64 exec, -1
.Lsel_p2_done:
	s_waitcnt lgkmcnt(0)
	v_lshlrev_b32_e32 v34, 7, v50
	v_sub_u32_e32 v44, 0x1f80, v34
	s_cmp_lg_u32 s31, 0
	s_cselect_b64 vcc, -1, 0
	v_cndmask_b32_e32 v34, v34, v44, vcc
	v_add_u32_e32 v34, s52, v34
	ds_read_b128 v[2:5], v34
	ds_read_b128 v[6:9], v34 offset:16
	ds_read_b128 v[10:13], v34 offset:32
	ds_read_b128 v[14:17], v34 offset:48
	ds_read_b128 v[18:21], v34 offset:64
	ds_read_b128 v[22:25], v34 offset:80
	ds_read_b128 v[26:29], v34 offset:96
	ds_read_b128 v[30:33], v34 offset:112
	s_waitcnt lgkmcnt(0)
	v_add_u32_e32 v35, v2, v3
	v_add3_u32 v35, v35, v4, v5
	v_add3_u32 v35, v35, v6, v7
	v_add3_u32 v35, v35, v8, v9
	v_add3_u32 v35, v35, v10, v11
	v_add3_u32 v35, v35, v12, v13
	v_add3_u32 v35, v35, v14, v15
	v_add3_u32 v35, v35, v16, v17
	v_add3_u32 v35, v35, v18, v19
	v_add3_u32 v35, v35, v20, v21
	v_add3_u32 v35, v35, v22, v23
	v_add3_u32 v35, v35, v24, v25
	v_add3_u32 v35, v35, v26, v27
	v_add3_u32 v35, v35, v28, v29
	v_add3_u32 v35, v35, v30, v31
	v_add3_u32 v35, v35, v32, v33
	v_mov_b32_e32 v36, v35
	s_nop 1
	v_add_u32_dpp v36, v36, v36 row_shr:1 row_mask:0xf bank_mask:0xf bound_ctrl:1
	s_nop 1
	v_add_u32_dpp v36, v36, v36 row_shr:2 row_mask:0xf bank_mask:0xf bound_ctrl:1
	s_nop 1
	v_add_u32_dpp v36, v36, v36 row_shr:4 row_mask:0xf bank_mask:0xf bound_ctrl:1
	s_nop 1
	v_add_u32_dpp v36, v36, v36 row_shr:8 row_mask:0xf bank_mask:0xf bound_ctrl:1
	s_nop 1
	v_add_u32_dpp v36, v36, v36 row_bcast:15 row_mask:0xa bank_mask:0xf
	s_nop 1
	v_add_u32_dpp v36, v36, v36 row_bcast:31 row_mask:0xc bank_mask:0xf
	s_nop 0
	v_readlane_b32 s4, v36, 63
	s_nop 1
	v_sub_u32_e32 v37, s4, v36
	v_add_u32_e32 v38, v37, v35
	v_cmp_gt_u32_e32 vcc, s15, v37
	v_cmp_le_u32_e64 s[4:5], s15, v38
	s_and_b64 s[4:5], vcc, s[4:5]
	s_ff1_i32_b64 s6, s[4:5]
	v_readlane_b32 s7, v37, s6
	s_lshl_b32 s10, s6, 7
	s_sub_i32 s11, 0x1f80, s10
	s_add_i32 s10, s10, 124
	s_cmp_lg_u32 s31, 0
	s_cselect_b32 s10, s11, s10
	s_cselect_b32 s34, 1, -1
	s_add_i32 s10, s10, s52
	v_and_b32_e32 v39, 31, v50
	v_lshlrev_b32_e32 v39, 2, v39
	v_mul_i32_i24_e32 v39, s34, v39
	v_add_u32_e32 v39, s10, v39
	ds_read_b32 v40, v39
	v_cmp_gt_u32_e32 vcc, 32, v50
	s_waitcnt lgkmcnt(0)
	s_nop 1
	v_cndmask_b32_e32 v40, 0, v40, vcc
	v_mov_b32_e32 v41, v40
	s_nop 1
	v_add_u32_dpp v41, v41, v41 row_shr:1 row_mask:0xf bank_mask:0xf bound_ctrl:1
	s_nop 1
	v_add_u32_dpp v41, v41, v41 row_shr:2 row_mask:0xf bank_mask:0xf bound_ctrl:1
	s_nop 1
	v_add_u32_dpp v41, v41, v41 row_shr:4 row_mask:0xf bank_mask:0xf bound_ctrl:1
	s_nop 1
	v_add_u32_dpp v41, v41, v41 row_shr:8 row_mask:0xf bank_mask:0xf bound_ctrl:1
	s_nop 1
	v_add_u32_dpp v41, v41, v41 row_bcast:15 row_mask:0xa bank_mask:0xf
	s_nop 1
	v_add_u32_dpp v41, v41, v41 row_bcast:31 row_mask:0xc bank_mask:0xf
	s_nop 0
	v_sub_u32_e32 v42, v41, v40
	v_add_u32_e32 v42, s7, v42
	v_add_u32_e32 v43, v42, v40
	v_cmp_gt_u32_e32 vcc, s15, v42
	v_cmp_le_u32_e64 s[4:5], s15, v43
	s_and_b64 s[4:5], vcc, s[4:5]
	s_ff1_i32_b64 s11, s[4:5]
	v_readlane_b32 s29, v40, s11
	v_readlane_b32 s5, v42, s11
	s_lshl_b32 s28, s6, 5
	s_sub_i32 s4, 31, s11
	s_add_i32 s28, s28, s4
	s_sub_i32 s15, s15, s5
	s_sub_i32 s5, 0x7ff, s28
	s_cmp_lg_u32 s31, 0
	s_cselect_b32 s33, s5, s28
	s_lshl_b32 s4, s13, 11
	s_or_b32 s78, s4, s33
	s_lshl_b32 s4, s30, 11
	s_or_b32 s17, s4, s28
	ds_write_b128 v64, v[150:153]
	ds_write_b128 v64, v[150:153] offset:1024
	ds_write_b128 v64, v[150:153] offset:2048
	ds_write_b128 v64, v[150:153] offset:3072
	s_cmp_lg_u32 s25, 0
	s_cbranch_scc0 .Lsel_p3_row
	s_mov_b32 s10, 0
.Lsel_p3_loop:
	v_add_u32_e32 v34, s10, v50
	v_cmpx_gt_u32_e32 vcc, s14, v34
	v_lshl_add_u32 v35, v34, 2, s52
	ds_read_b32 v36, v35 offset:8192
	s_waitcnt lgkmcnt(0)
	v_lshrrev_b32_e32 v37, 10, v36
	v_cmpx_eq_u32_e32 vcc, s78, v37
	v_and_b32_e32 v37, 0x3ff, v36
	v_lshl_add_u32 v37, v37, 2, s52
	ds_add_u32 v37, v57
	s_mov_b64 exec, -1
	s_add_i32 s10, s10, 64
	s_cmp_lt_u32 s10, s14
	s_cbranch_scc1 .Lsel_p3_loop
	s_branch .Lsel_p3_done

.Lsel_p3_rloop:
	v_add_u32_e32 v34, s10, v50
	v_cmpx_gt_i32_e32 vcc, s2, v34
	v_lshlrev_b32_e32 v35, 2, v34
	global_load_dword v36, v35, s[42:43]
	s_waitcnt vmcnt(0)
	v_lshrrev_b32_e32 v37, 10, v36
	v_cmpx_eq_u32_e32 vcc, s78, v37
	v_and_b32_e32 v37, 0x3ff, v36
	v_lshl_add_u32 v37, v37, 2, s52
	ds_add_u32 v37, v57
	s_mov_b64 exec, -1
	s_add_i32 s10, s10, 64
	s_cmp_lt_i32 s10, s2
	s_cbranch_scc1 .Lsel_p3_rloop
.Lsel_p3_done:
	s_waitcnt lgkmcnt(0)
	v_lshlrev_b32_e32 v34, 6, v50
	v_sub_u32_e32 v44, 0xfc0, v34
	s_cmp_lg_u32 s31, 0
	s_cselect_b64 vcc, -1, 0
	v_cndmask_b32_e32 v34, v34, v44, vcc
	v_add_u32_e32 v34, s52, v34
	ds_read_b128 v[2:5], v34
	ds_read_b128 v[6:9], v34 offset:16
	ds_read_b128 v[10:13], v34 offset:32
	ds_read_b128 v[14:17], v34 offset:48
	s_waitcnt lgkmcnt(0)
	v_add_u32_e32 v35, v2, v3
	v_add3_u32 v35, v35, v4, v5
	v_add3_u32 v35, v35, v6, v7
	v_add3_u32 v35, v35, v8, v9
	v_add3_u32 v35, v35, v10, v11
	v_add3_u32 v35, v35, v12, v13
	v_add3_u32 v35, v35, v14, v15
	v_add3_u32 v35, v35, v16, v17
	v_mov_b32_e32 v36, v35
	s_nop 1
	v_add_u32_dpp v36, v36, v36 row_shr:1 row_mask:0xf bank_mask:0xf bound_ctrl:1
	s_nop 1
	v_add_u32_dpp v36, v36, v36 row_shr:2 row_mask:0xf bank_mask:0xf bound_ctrl:1
	s_nop 1
	v_add_u32_dpp v36, v36, v36 row_shr:4 row_mask:0xf bank_mask:0xf bound_ctrl:1
	s_nop 1
	v_add_u32_dpp v36, v36, v36 row_shr:8 row_mask:0xf bank_mask:0xf bound_ctrl:1
	s_nop 1
	v_add_u32_dpp v36, v36, v36 row_bcast:15 row_mask:0xa bank_mask:0xf
	s_nop 1
	v_add_u32_dpp v36, v36, v36 row_bcast:31 row_mask:0xc bank_mask:0xf
	s_nop 0
	v_readlane_b32 s4, v36, 63
	s_nop 1
	v_sub_u32_e32 v37, s4, v36
	v_add_u32_e32 v38, v37, v35
	v_cmp_gt_u32_e32 vcc, s15, v37
	v_cmp_le_u32_e64 s[4:5], s15, v38
	s_and_b64 s[4:5], vcc, s[4:5]
	s_ff1_i32_b64 s6, s[4:5]
	v_readlane_b32 s7, v37, s6
	s_lshl_b32 s10, s6, 6
	s_sub_i32 s11, 0xfc0, s10
	s_add_i32 s10, s10, 60
	s_cmp_lg_u32 s31, 0
	s_cselect_b32 s10, s11, s10
	s_cselect_b32 s34, 1, -1
	s_add_i32 s10, s10, s52
	v_and_b32_e32 v39, 15, v50
	v_lshlrev_b32_e32 v39, 2, v39
	v_mul_i32_i24_e32 v39, s34, v39
	v_add_u32_e32 v39, s10, v39
	ds_read_b32 v40, v39
	v_cmp_gt_u32_e32 vcc, 16, v50
	s_waitcnt lgkmcnt(0)
	s_nop 1
	v_cndmask_b32_e32 v40, 0, v40, vcc
	v_mov_b32_e32 v41, v40
	s_nop 1
	v_add_u32_dpp v41, v41, v41 row_shr:1 row_mask:0xf bank_mask:0xf bound_ctrl:1
	s_nop 1
	v_add_u32_dpp v41, v41, v41 row_shr:2 row_mask:0xf bank_mask:0xf bound_ctrl:1
	s_nop 1
	v_add_u32_dpp v41, v41, v41 row_shr:4 row_mask:0xf bank_mask:0xf bound_ctrl:1
	s_nop 1
	v_add_u32_dpp v41, v41, v41 row_shr:8 row_mask:0xf bank_mask:0xf bound_ctrl:1
	s_nop 1
	v_add_u32_dpp v41, v41, v41 row_bcast:15 row_mask:0xa bank_mask:0xf
	s_nop 1
	v_add_u32_dpp v41, v41, v41 row_bcast:31 row_mask:0xc bank_mask:0xf
	s_nop 0
	v_sub_u32_e32 v42, v41, v40
	v_add_u32_e32 v42, s7, v42
	v_add_u32_e32 v43, v42, v40
	v_cmp_gt_u32_e32 vcc, s15, v42
	v_cmp_le_u32_e64 s[4:5], s15, v43
	s_and_b64 s[4:5], vcc, s[4:5]
	s_ff1_i32_b64 s11, s[4:5]
	v_readlane_b32 s29, v40, s11
	v_readlane_b32 s5, v42, s11
	s_lshl_b32 s28, s6, 4
	s_sub_i32 s4, 15, s11
	s_add_i32 s28, s28, s4
	s_sub_i32 s15, s15, s5
	s_sub_i32 s5, 0x3ff, s28
	s_cmp_lg_u32 s31, 0
	s_cselect_b32 s5, s5, s28
	s_lshl_b32 s76, s78, 10
	s_or_b32 s76, s76, s5
	s_lshl_b32 s17, s17, 10
	s_or_b32 s17, s17, s28
	s_mov_b32 s26, 0
	s_mov_b32 s27, 0
	s_cmp_eq_u32 s15, s29
	s_cbranch_scc1 .Lsel_simple
	s_mov_b64 s[8:9], s[42:43]
	global_load_dwordx4 v[2:5], v58, s[8:9]
	global_load_dwordx4 v[6:9], v58, s[8:9] offset:1024
	global_load_dwordx4 v[10:13], v58, s[8:9] offset:2048
	global_load_dwordx4 v[14:17], v58, s[8:9] offset:3072
	s_mov_b32 s16, 0
	s_waitcnt vmcnt(0)

.Lsel_simple:
	s_cmp_lg_u32 s31, 0
	s_cbranch_scc1 .Lsel_simple_neg
	s_mov_b64 s[8:9], s[42:43]
	global_load_dwordx4 v[2:5], v58, s[8:9]
	global_load_dwordx4 v[6:9], v58, s[8:9] offset:1024
	global_load_dwordx4 v[10:13], v58, s[8:9] offset:2048
	global_load_dwordx4 v[14:17], v58, s[8:9] offset:3072
	s_mov_b32 s16, 0
	s_waitcnt vmcnt(0)

.Lsel_fsp_nold:
	s_cmp_le_i32 s36, s2
	s_cbranch_scc0 .Lsel_fsp_tail
	v_add_u32_e32 v145, s16, v56
	v_cmp_ge_i32_e64 s[58:59], v18, s76
	v_cmp_ge_i32_e64 s[60:61], v19, s76
	v_cmp_ge_i32_e64 s[62:63], v20, s76
	v_cmp_ge_i32_e64 s[64:65], v21, s76
	v_mov_b32_e32 v135, s26
	v_mbcnt_lo_u32_b32 v135, s58, v135
	v_mbcnt_hi_u32_b32 v135, s59, v135
	v_mbcnt_lo_u32_b32 v135, s60, v135
	v_mbcnt_hi_u32_b32 v135, s61, v135
	v_mbcnt_lo_u32_b32 v135, s62, v135
	v_mbcnt_hi_u32_b32 v135, s63, v135
	v_mbcnt_lo_u32_b32 v135, s64, v135
	v_mbcnt_hi_u32_b32 v135, s65, v135
	v_lshlrev_b32_e32 v135, 2, v135
	s_mov_b64 exec, s[58:59]
	v_add_u32_e32 v141, 0, v145
	global_store_dword v135, v141, s[40:41]
	v_add_u32_e32 v135, 4, v135
	s_mov_b64 exec, s[60:61]
	v_add_u32_e32 v142, 1, v145
	global_store_dword v135, v142, s[40:41]
	v_add_u32_e32 v135, 4, v135
	s_mov_b64 exec, s[62:63]
	v_add_u32_e32 v143, 2, v145
	global_store_dword v135, v143, s[40:41]
	v_add_u32_e32 v135, 4, v135
	s_mov_b64 exec, s[64:65]
	v_add_u32_e32 v144, 3, v145
	global_store_dword v135, v144, s[40:41]
	v_add_u32_e32 v135, 4, v135
	s_mov_b64 exec, -1
	s_bcnt1_i32_b64 s4, s[58:59]
	s_add_i32 s26, s26, s4
	s_bcnt1_i32_b64 s4, s[60:61]
	s_add_i32 s26, s26, s4
	s_bcnt1_i32_b64 s4, s[62:63]
	s_add_i32 s26, s26, s4
	s_bcnt1_i32_b64 s4, s[64:65]
	s_add_i32 s26, s26, s4
	v_cmp_ge_i32_e64 s[58:59], v22, s76
	v_cmp_ge_i32_e64 s[60:61], v23, s76
	v_cmp_ge_i32_e64 s[62:63], v24, s76
	v_cmp_ge_i32_e64 s[64:65], v25, s76
	v_mov_b32_e32 v135, s26
	v_mbcnt_lo_u32_b32 v135, s58, v135
	v_mbcnt_hi_u32_b32 v135, s59, v135
	v_mbcnt_lo_u32_b32 v135, s60, v135
	v_mbcnt_hi_u32_b32 v135, s61, v135
	v_mbcnt_lo_u32_b32 v135, s62, v135
	v_mbcnt_hi_u32_b32 v135, s63, v135
	v_mbcnt_lo_u32_b32 v135, s64, v135
	v_mbcnt_hi_u32_b32 v135, s65, v135
	v_lshlrev_b32_e32 v135, 2, v135
	s_mov_b64 exec, s[58:59]
	v_add_u32_e32 v141, 0x100, v145
	global_store_dword v135, v141, s[40:41]
	v_add_u32_e32 v135, 4, v135
	s_mov_b64 exec, s[60:61]
	v_add_u32_e32 v142, 0x101, v145
	global_store_dword v135, v142, s[40:41]
	v_add_u32_e32 v135, 4, v135
	s_mov_b64 exec, s[62:63]
	v_add_u32_e32 v143, 0x102, v145
	global_store_dword v135, v143, s[40:41]
	v_add_u32_e32 v135, 4, v135
	s_mov_b64 exec, s[64:65]
	v_add_u32_e32 v144, 0x103, v145
	global_store_dword v135, v144, s[40:41]
	v_add_u32_e32 v135, 4, v135
	s_mov_b64 exec, -1
	s_bcnt1_i32_b64 s4, s[58:59]
	s_add_i32 s26, s26, s4
	s_bcnt1_i32_b64 s4, s[60:61]
	s_add_i32 s26, s26, s4
	s_bcnt1_i32_b64 s4, s[62:63]
	s_add_i32 s26, s26, s4
	s_bcnt1_i32_b64 s4, s[64:65]
	s_add_i32 s26, s26, s4
	v_cmp_ge_i32_e64 s[58:59], v26, s76
	v_cmp_ge_i32_e64 s[60:61], v27, s76
	v_cmp_ge_i32_e64 s[62:63], v28, s76
	v_cmp_ge_i32_e64 s[64:65], v29, s76
	v_mov_b32_e32 v135, s26
	v_mbcnt_lo_u32_b32 v135, s58, v135
	v_mbcnt_hi_u32_b32 v135, s59, v135
	v_mbcnt_lo_u32_b32 v135, s60, v135
	v_mbcnt_hi_u32_b32 v135, s61, v135
	v_mbcnt_lo_u32_b32 v135, s62, v135
	v_mbcnt_hi_u32_b32 v135, s63, v135
	v_mbcnt_lo_u32_b32 v135, s64, v135
	v_mbcnt_hi_u32_b32 v135, s65, v135
	v_lshlrev_b32_e32 v135, 2, v135
	s_mov_b64 exec, s[58:59]
	v_add_u32_e32 v141, 0x200, v145
	global_store_dword v135, v141, s[40:41]
	v_add_u32_e32 v135, 4, v135
	s_mov_b64 exec, s[60:61]
	v_add_u32_e32 v142, 0x201, v145
	global_store_dword v135, v142, s[40:41]
	v_add_u32_e32 v135, 4, v135
	s_mov_b64 exec, s[62:63]
	v_add_u32_e32 v143, 0x202, v145
	global_store_dword v135, v143, s[40:41]
	v_add_u32_e32 v135, 4, v135
	s_mov_b64 exec, s[64:65]
	v_add_u32_e32 v144, 0x203, v145
	global_store_dword v135, v144, s[40:41]
	v_add_u32_e32 v135, 4, v135
	s_mov_b64 exec, -1
	s_bcnt1_i32_b64 s4, s[58:59]
	s_add_i32 s26, s26, s4
	s_bcnt1_i32_b64 s4, s[60:61]
	s_add_i32 s26, s26, s4
	s_bcnt1_i32_b64 s4, s[62:63]
	s_add_i32 s26, s26, s4
	s_bcnt1_i32_b64 s4, s[64:65]
	s_add_i32 s26, s26, s4
	v_cmp_ge_i32_e64 s[58:59], v30, s76
	v_cmp_ge_i32_e64 s[60:61], v31, s76
	v_cmp_ge_i32_e64 s[62:63], v32, s76
	v_cmp_ge_i32_e64 s[64:65], v33, s76
	v_mov_b32_e32 v135, s26
	v_mbcnt_lo_u32_b32 v135, s58, v135
	v_mbcnt_hi_u32_b32 v135, s59, v135
	v_mbcnt_lo_u32_b32 v135, s60, v135
	v_mbcnt_hi_u32_b32 v135, s61, v135
	v_mbcnt_lo_u32_b32 v135, s62, v135
	v_mbcnt_hi_u32_b32 v135, s63, v135
	v_mbcnt_lo_u32_b32 v135, s64, v135
	v_mbcnt_hi_u32_b32 v135, s65, v135
	v_lshlrev_b32_e32 v135, 2, v135
	s_mov_b64 exec, s[58:59]
	v_add_u32_e32 v141, 0x300, v145
	global_store_dword v135, v141, s[40:41]
	v_add_u32_e32 v135, 4, v135
	s_mov_b64 exec, s[60:61]
	v_add_u32_e32 v142, 0x301, v145
	global_store_dword v135, v142, s[40:41]
	v_add_u32_e32 v135, 4, v135
	s_mov_b64 exec, s[62:63]
	v_add_u32_e32 v143, 0x302, v145
	global_store_dword v135, v143, s[40:41]
	v_add_u32_e32 v135, 4, v135
	s_mov_b64 exec, s[64:65]
	v_add_u32_e32 v144, 0x303, v145
	global_store_dword v135, v144, s[40:41]
	v_add_u32_e32 v135, 4, v135
	s_mov_b64 exec, -1
	s_bcnt1_i32_b64 s4, s[58:59]
	s_add_i32 s26, s26, s4
	s_bcnt1_i32_b64 s4, s[60:61]
	s_add_i32 s26, s26, s4
	s_bcnt1_i32_b64 s4, s[62:63]
	s_add_i32 s26, s26, s4
	s_bcnt1_i32_b64 s4, s[64:65]
	s_add_i32 s26, s26, s4
	s_mov_b32 s16, s36
	s_cmp_lt_i32 s16, s2
	s_cbranch_scc0 .Lsel_fsp_done
	s_waitcnt vmcnt(16)
	s_branch .Lsel_fsp_loop
.Lsel_fsp_tail:
	s_sub_i32 s37, s2, s16
	v_sub_u32_e32 v134, s37, v56
	v_add_u32_e32 v145, s16, v56
	v_cmpx_lt_i32_e32 vcc, 0, v134
	v_cmp_ge_i32_e64 s[58:59], v18, s76
	v_cmpx_lt_i32_e32 vcc, 1, v134
	v_cmp_ge_i32_e64 s[60:61], v19, s76
	v_cmpx_lt_i32_e32 vcc, 2, v134
	v_cmp_ge_i32_e64 s[62:63], v20, s76
	v_cmpx_lt_i32_e32 vcc, 3, v134
	v_cmp_ge_i32_e64 s[64:65], v21, s76
	s_mov_b64 exec, -1
	v_mov_b32_e32 v135, s26
	v_mbcnt_lo_u32_b32 v135, s58, v135
	v_mbcnt_hi_u32_b32 v135, s59, v135
	v_mbcnt_lo_u32_b32 v135, s60, v135
	v_mbcnt_hi_u32_b32 v135, s61, v135
	v_mbcnt_lo_u32_b32 v135, s62, v135
	v_mbcnt_hi_u32_b32 v135, s63, v135
	v_mbcnt_lo_u32_b32 v135, s64, v135
	v_mbcnt_hi_u32_b32 v135, s65, v135
	v_lshlrev_b32_e32 v135, 2, v135
	s_mov_b64 exec, s[58:59]
	v_add_u32_e32 v141, 0, v145
	global_store_dword v135, v141, s[40:41]
	v_add_u32_e32 v135, 4, v135
	s_mov_b64 exec, s[60:61]
	v_add_u32_e32 v142, 1, v145
	global_store_dword v135, v142, s[40:41]
	v_add_u32_e32 v135, 4, v135
	s_mov_b64 exec, s[62:63]
	v_add_u32_e32 v143, 2, v145
	global_store_dword v135, v143, s[40:41]
	v_add_u32_e32 v135, 4, v135
	s_mov_b64 exec, s[64:65]
	v_add_u32_e32 v144, 3, v145
	global_store_dword v135, v144, s[40:41]
	v_add_u32_e32 v135, 4, v135
	s_mov_b64 exec, -1
	s_bcnt1_i32_b64 s4, s[58:59]
	s_add_i32 s26, s26, s4
	s_bcnt1_i32_b64 s4, s[60:61]
	s_add_i32 s26, s26, s4
	s_bcnt1_i32_b64 s4, s[62:63]
	s_add_i32 s26, s26, s4
	s_bcnt1_i32_b64 s4, s[64:65]
	s_add_i32 s26, s26, s4
	v_cmpx_lt_i32_e32 vcc, 0x100, v134
	v_cmp_ge_i32_e64 s[58:59], v22, s76
	v_cmpx_lt_i32_e32 vcc, 0x101, v134
	v_cmp_ge_i32_e64 s[60:61], v23, s76
	v_cmpx_lt_i32_e32 vcc, 0x102, v134
	v_cmp_ge_i32_e64 s[62:63], v24, s76
	v_cmpx_lt_i32_e32 vcc, 0x103, v134
	v_cmp_ge_i32_e64 s[64:65], v25, s76
	s_mov_b64 exec, -1
	v_mov_b32_e32 v135, s26
	v_mbcnt_lo_u32_b32 v135, s58, v135
	v_mbcnt_hi_u32_b32 v135, s59, v135
	v_mbcnt_lo_u32_b32 v135, s60, v135
	v_mbcnt_hi_u32_b32 v135, s61, v135
	v_mbcnt_lo_u32_b32 v135, s62, v135
	v_mbcnt_hi_u32_b32 v135, s63, v135
	v_mbcnt_lo_u32_b32 v135, s64, v135
	v_mbcnt_hi_u32_b32 v135, s65, v135
	v_lshlrev_b32_e32 v135, 2, v135
	s_mov_b64 exec, s[58:59]
	v_add_u32_e32 v141, 0x100, v145
	global_store_dword v135, v141, s[40:41]
	v_add_u32_e32 v135, 4, v135
	s_mov_b64 exec, s[60:61]
	v_add_u32_e32 v142, 0x101, v145
	global_store_dword v135, v142, s[40:41]
	v_add_u32_e32 v135, 4, v135
	s_mov_b64 exec, s[62:63]
	v_add_u32_e32 v143, 0x102, v145
	global_store_dword v135, v143, s[40:41]
	v_add_u32_e32 v135, 4, v135
	s_mov_b64 exec, s[64:65]
	v_add_u32_e32 v144, 0x103, v145
	global_store_dword v135, v144, s[40:41]
	v_add_u32_e32 v135, 4, v135
	s_mov_b64 exec, -1
	s_bcnt1_i32_b64 s4, s[58:59]
	s_add_i32 s26, s26, s4
	s_bcnt1_i32_b64 s4, s[60:61]
	s_add_i32 s26, s26, s4
	s_bcnt1_i32_b64 s4, s[62:63]
	s_add_i32 s26, s26, s4
	s_bcnt1_i32_b64 s4, s[64:65]
	s_add_i32 s26, s26, s4
	v_cmpx_lt_i32_e32 vcc, 0x200, v134
	v_cmp_ge_i32_e64 s[58:59], v26, s76
	v_cmpx_lt_i32_e32 vcc, 0x201, v134
	v_cmp_ge_i32_e64 s[60:61], v27, s76
	v_cmpx_lt_i32_e32 vcc, 0x202, v134
	v_cmp_ge_i32_e64 s[62:63], v28, s76
	v_cmpx_lt_i32_e32 vcc, 0x203, v134
	v_cmp_ge_i32_e64 s[64:65], v29, s76
	s_mov_b64 exec, -1
	v_mov_b32_e32 v135, s26
	v_mbcnt_lo_u32_b32 v135, s58, v135
	v_mbcnt_hi_u32_b32 v135, s59, v135
	v_mbcnt_lo_u32_b32 v135, s60, v135
	v_mbcnt_hi_u32_b32 v135, s61, v135
	v_mbcnt_lo_u32_b32 v135, s62, v135
	v_mbcnt_hi_u32_b32 v135, s63, v135
	v_mbcnt_lo_u32_b32 v135, s64, v135
	v_mbcnt_hi_u32_b32 v135, s65, v135
	v_lshlrev_b32_e32 v135, 2, v135
	s_mov_b64 exec, s[58:59]
	v_add_u32_e32 v141, 0x200, v145
	global_store_dword v135, v141, s[40:41]
	v_add_u32_e32 v135, 4, v135
	s_mov_b64 exec, s[60:61]
	v_add_u32_e32 v142, 0x201, v145
	global_store_dword v135, v142, s[40:41]
	v_add_u32_e32 v135, 4, v135
	s_mov_b64 exec, s[62:63]
	v_add_u32_e32 v143, 0x202, v145
	global_store_dword v135, v143, s[40:41]
	v_add_u32_e32 v135, 4, v135
	s_mov_b64 exec, s[64:65]
	v_add_u32_e32 v144, 0x203, v145
	global_store_dword v135, v144, s[40:41]
	v_add_u32_e32 v135, 4, v135
	s_mov_b64 exec, -1
	s_bcnt1_i32_b64 s4, s[58:59]
	s_add_i32 s26, s26, s4
	s_bcnt1_i32_b64 s4, s[60:61]
	s_add_i32 s26, s26, s4
	s_bcnt1_i32_b64 s4, s[62:63]
	s_add_i32 s26, s26, s4
	s_bcnt1_i32_b64 s4, s[64:65]
	s_add_i32 s26, s26, s4
	v_cmpx_lt_i32_e32 vcc, 0x300, v134
	v_cmp_ge_i32_e64 s[58:59], v30, s76
	v_cmpx_lt_i32_e32 vcc, 0x301, v134
	v_cmp_ge_i32_e64 s[60:61], v31, s76
	v_cmpx_lt_i32_e32 vcc, 0x302, v134
	v_cmp_ge_i32_e64 s[62:63], v32, s76
	v_cmpx_lt_i32_e32 vcc, 0x303, v134
	v_cmp_ge_i32_e64 s[64:65], v33, s76
	s_mov_b64 exec, -1
	v_mov_b32_e32 v135, s26
	v_mbcnt_lo_u32_b32 v135, s58, v135
	v_mbcnt_hi_u32_b32 v135, s59, v135
	v_mbcnt_lo_u32_b32 v135, s60, v135
	v_mbcnt_hi_u32_b32 v135, s61, v135
	v_mbcnt_lo_u32_b32 v135, s62, v135
	v_mbcnt_hi_u32_b32 v135, s63, v135
	v_mbcnt_lo_u32_b32 v135, s64, v135
	v_mbcnt_hi_u32_b32 v135, s65, v135
	v_lshlrev_b32_e32 v135, 2, v135
	s_mov_b64 exec, s[58:59]
	v_add_u32_e32 v141, 0x300, v145
	global_store_dword v135, v141, s[40:41]
	v_add_u32_e32 v135, 4, v135
	s_mov_b64 exec, s[60:61]
	v_add_u32_e32 v142, 0x301, v145
	global_store_dword v135, v142, s[40:41]
	v_add_u32_e32 v135, 4, v135
	s_mov_b64 exec, s[62:63]
	v_add_u32_e32 v143, 0x302, v145
	global_store_dword v135, v143, s[40:41]
	v_add_u32_e32 v135, 4, v135
	s_mov_b64 exec, s[64:65]
	v_add_u32_e32 v144, 0x303, v145
	global_store_dword v135, v144, s[40:41]
	v_add_u32_e32 v135, 4, v135
	s_mov_b64 exec, -1
	s_bcnt1_i32_b64 s4, s[58:59]
	s_add_i32 s26, s26, s4
	s_bcnt1_i32_b64 s4, s[60:61]
	s_add_i32 s26, s26, s4
	s_bcnt1_i32_b64 s4, s[62:63]
	s_add_i32 s26, s26, s4
	s_bcnt1_i32_b64 s4, s[64:65]
	s_add_i32 s26, s26, s4

.Lsel_fsn_nold:
	s_cmp_le_i32 s36, s2
	s_cbranch_scc0 .Lsel_fsn_tail
	v_add_u32_e32 v145, s16, v56
	v_cmp_le_u32_e64 s[58:59], v18, s76
	v_cmp_le_u32_e64 s[60:61], v19, s76
	v_cmp_le_u32_e64 s[62:63], v20, s76
	v_cmp_le_u32_e64 s[64:65], v21, s76
	v_mov_b32_e32 v135, s26
	v_mbcnt_lo_u32_b32 v135, s58, v135
	v_mbcnt_hi_u32_b32 v135, s59, v135
	v_mbcnt_lo_u32_b32 v135, s60, v135
	v_mbcnt_hi_u32_b32 v135, s61, v135
	v_mbcnt_lo_u32_b32 v135, s62, v135
	v_mbcnt_hi_u32_b32 v135, s63, v135
	v_mbcnt_lo_u32_b32 v135, s64, v135
	v_mbcnt_hi_u32_b32 v135, s65, v135
	v_lshlrev_b32_e32 v135, 2, v135
	s_mov_b64 exec, s[58:59]
	v_add_u32_e32 v141, 0, v145
	global_store_dword v135, v141, s[40:41]
	v_add_u32_e32 v135, 4, v135
	s_mov_b64 exec, s[60:61]
	v_add_u32_e32 v142, 1, v145
	global_store_dword v135, v142, s[40:41]
	v_add_u32_e32 v135, 4, v135
	s_mov_b64 exec, s[62:63]
	v_add_u32_e32 v143, 2, v145
	global_store_dword v135, v143, s[40:41]
	v_add_u32_e32 v135, 4, v135
	s_mov_b64 exec, s[64:65]
	v_add_u32_e32 v144, 3, v145
	global_store_dword v135, v144, s[40:41]
	v_add_u32_e32 v135, 4, v135
	s_mov_b64 exec, -1
	s_bcnt1_i32_b64 s4, s[58:59]
	s_add_i32 s26, s26, s4
	s_bcnt1_i32_b64 s4, s[60:61]
	s_add_i32 s26, s26, s4
	s_bcnt1_i32_b64 s4, s[62:63]
	s_add_i32 s26, s26, s4
	s_bcnt1_i32_b64 s4, s[64:65]
	s_add_i32 s26, s26, s4
	v_cmp_le_u32_e64 s[58:59], v22, s76
	v_cmp_le_u32_e64 s[60:61], v23, s76
	v_cmp_le_u32_e64 s[62:63], v24, s76
	v_cmp_le_u32_e64 s[64:65], v25, s76
	v_mov_b32_e32 v135, s26
	v_mbcnt_lo_u32_b32 v135, s58, v135
	v_mbcnt_hi_u32_b32 v135, s59, v135
	v_mbcnt_lo_u32_b32 v135, s60, v135
	v_mbcnt_hi_u32_b32 v135, s61, v135
	v_mbcnt_lo_u32_b32 v135, s62, v135
	v_mbcnt_hi_u32_b32 v135, s63, v135
	v_mbcnt_lo_u32_b32 v135, s64, v135
	v_mbcnt_hi_u32_b32 v135, s65, v135
	v_lshlrev_b32_e32 v135, 2, v135
	s_mov_b64 exec, s[58:59]
	v_add_u32_e32 v141, 0x100, v145
	global_store_dword v135, v141, s[40:41]
	v_add_u32_e32 v135, 4, v135
	s_mov_b64 exec, s[60:61]
	v_add_u32_e32 v142, 0x101, v145
	global_store_dword v135, v142, s[40:41]
	v_add_u32_e32 v135, 4, v135
	s_mov_b64 exec, s[62:63]
	v_add_u32_e32 v143, 0x102, v145
	global_store_dword v135, v143, s[40:41]
	v_add_u32_e32 v135, 4, v135
	s_mov_b64 exec, s[64:65]
	v_add_u32_e32 v144, 0x103, v145
	global_store_dword v135, v144, s[40:41]
	v_add_u32_e32 v135, 4, v135
	s_mov_b64 exec, -1
	s_bcnt1_i32_b64 s4, s[58:59]
	s_add_i32 s26, s26, s4
	s_bcnt1_i32_b64 s4, s[60:61]
	s_add_i32 s26, s26, s4
	s_bcnt1_i32_b64 s4, s[62:63]
	s_add_i32 s26, s26, s4
	s_bcnt1_i32_b64 s4, s[64:65]
	s_add_i32 s26, s26, s4
	v_cmp_le_u32_e64 s[58:59], v26, s76
	v_cmp_le_u32_e64 s[60:61], v27, s76
	v_cmp_le_u32_e64 s[62:63], v28, s76
	v_cmp_le_u32_e64 s[64:65], v29, s76
	v_mov_b32_e32 v135, s26
	v_mbcnt_lo_u32_b32 v135, s58, v135
	v_mbcnt_hi_u32_b32 v135, s59, v135
	v_mbcnt_lo_u32_b32 v135, s60, v135
	v_mbcnt_hi_u32_b32 v135, s61, v135
	v_mbcnt_lo_u32_b32 v135, s62, v135
	v_mbcnt_hi_u32_b32 v135, s63, v135
	v_mbcnt_lo_u32_b32 v135, s64, v135
	v_mbcnt_hi_u32_b32 v135, s65, v135
	v_lshlrev_b32_e32 v135, 2, v135
	s_mov_b64 exec, s[58:59]
	v_add_u32_e32 v141, 0x200, v145
	global_store_dword v135, v141, s[40:41]
	v_add_u32_e32 v135, 4, v135
	s_mov_b64 exec, s[60:61]
	v_add_u32_e32 v142, 0x201, v145
	global_store_dword v135, v142, s[40:41]
	v_add_u32_e32 v135, 4, v135
	s_mov_b64 exec, s[62:63]
	v_add_u32_e32 v143, 0x202, v145
	global_store_dword v135, v143, s[40:41]
	v_add_u32_e32 v135, 4, v135
	s_mov_b64 exec, s[64:65]
	v_add_u32_e32 v144, 0x203, v145
	global_store_dword v135, v144, s[40:41]
	v_add_u32_e32 v135, 4, v135
	s_mov_b64 exec, -1
	s_bcnt1_i32_b64 s4, s[58:59]
	s_add_i32 s26, s26, s4
	s_bcnt1_i32_b64 s4, s[60:61]
	s_add_i32 s26, s26, s4
	s_bcnt1_i32_b64 s4, s[62:63]
	s_add_i32 s26, s26, s4
	s_bcnt1_i32_b64 s4, s[64:65]
	s_add_i32 s26, s26, s4
	v_cmp_le_u32_e64 s[58:59], v30, s76
	v_cmp_le_u32_e64 s[60:61], v31, s76
	v_cmp_le_u32_e64 s[62:63], v32, s76
	v_cmp_le_u32_e64 s[64:65], v33, s76
	v_mov_b32_e32 v135, s26
	v_mbcnt_lo_u32_b32 v135, s58, v135
	v_mbcnt_hi_u32_b32 v135, s59, v135
	v_mbcnt_lo_u32_b32 v135, s60, v135
	v_mbcnt_hi_u32_b32 v135, s61, v135
	v_mbcnt_lo_u32_b32 v135, s62, v135
	v_mbcnt_hi_u32_b32 v135, s63, v135
	v_mbcnt_lo_u32_b32 v135, s64, v135
	v_mbcnt_hi_u32_b32 v135, s65, v135
	v_lshlrev_b32_e32 v135, 2, v135
	s_mov_b64 exec, s[58:59]
	v_add_u32_e32 v141, 0x300, v145
	global_store_dword v135, v141, s[40:41]
	v_add_u32_e32 v135, 4, v135
	s_mov_b64 exec, s[60:61]
	v_add_u32_e32 v142, 0x301, v145
	global_store_dword v135, v142, s[40:41]
	v_add_u32_e32 v135, 4, v135
	s_mov_b64 exec, s[62:63]
	v_add_u32_e32 v143, 0x302, v145
	global_store_dword v135, v143, s[40:41]
	v_add_u32_e32 v135, 4, v135
	s_mov_b64 exec, s[64:65]
	v_add_u32_e32 v144, 0x303, v145
	global_store_dword v135, v144, s[40:41]
	v_add_u32_e32 v135, 4, v135
	s_mov_b64 exec, -1
	s_bcnt1_i32_b64 s4, s[58:59]
	s_add_i32 s26, s26, s4
	s_bcnt1_i32_b64 s4, s[60:61]
	s_add_i32 s26, s26, s4
	s_bcnt1_i32_b64 s4, s[62:63]
	s_add_i32 s26, s26, s4
	s_bcnt1_i32_b64 s4, s[64:65]
	s_add_i32 s26, s26, s4
	s_mov_b32 s16, s36
	s_cmp_lt_i32 s16, s2
	s_cbranch_scc0 .Lsel_fsn_done
	s_waitcnt vmcnt(16)
	s_branch .Lsel_fsn_loop
.Lsel_fsn_tail:
	s_sub_i32 s37, s2, s16
	v_sub_u32_e32 v134, s37, v56
	v_add_u32_e32 v145, s16, v56
	v_cmpx_lt_i32_e32 vcc, 0, v134
	v_cmp_le_u32_e64 s[58:59], v18, s76
	v_cmpx_lt_i32_e32 vcc, 1, v134
	v_cmp_le_u32_e64 s[60:61], v19, s76
	v_cmpx_lt_i32_e32 vcc, 2, v134
	v_cmp_le_u32_e64 s[62:63], v20, s76
	v_cmpx_lt_i32_e32 vcc, 3, v134
	v_cmp_le_u32_e64 s[64:65], v21, s76
	s_mov_b64 exec, -1
	v_mov_b32_e32 v135, s26
	v_mbcnt_lo_u32_b32 v135, s58, v135
	v_mbcnt_hi_u32_b32 v135, s59, v135
	v_mbcnt_lo_u32_b32 v135, s60, v135
	v_mbcnt_hi_u32_b32 v135, s61, v135
	v_mbcnt_lo_u32_b32 v135, s62, v135
	v_mbcnt_hi_u32_b32 v135, s63, v135
	v_mbcnt_lo_u32_b32 v135, s64, v135
	v_mbcnt_hi_u32_b32 v135, s65, v135
	v_lshlrev_b32_e32 v135, 2, v135
	s_mov_b64 exec, s[58:59]
	v_add_u32_e32 v141, 0, v145
	global_store_dword v135, v141, s[40:41]
	v_add_u32_e32 v135, 4, v135
	s_mov_b64 exec, s[60:61]
	v_add_u32_e32 v142, 1, v145
	global_store_dword v135, v142, s[40:41]
	v_add_u32_e32 v135, 4, v135
	s_mov_b64 exec, s[62:63]
	v_add_u32_e32 v143, 2, v145
	global_store_dword v135, v143, s[40:41]
	v_add_u32_e32 v135, 4, v135
	s_mov_b64 exec, s[64:65]
	v_add_u32_e32 v144, 3, v145
	global_store_dword v135, v144, s[40:41]
	v_add_u32_e32 v135, 4, v135
	s_mov_b64 exec, -1
	s_bcnt1_i32_b64 s4, s[58:59]
	s_add_i32 s26, s26, s4
	s_bcnt1_i32_b64 s4, s[60:61]
	s_add_i32 s26, s26, s4
	s_bcnt1_i32_b64 s4, s[62:63]
	s_add_i32 s26, s26, s4
	s_bcnt1_i32_b64 s4, s[64:65]
	s_add_i32 s26, s26, s4
	v_cmpx_lt_i32_e32 vcc, 0x100, v134
	v_cmp_le_u32_e64 s[58:59], v22, s76
	v_cmpx_lt_i32_e32 vcc, 0x101, v134
	v_cmp_le_u32_e64 s[60:61], v23, s76
	v_cmpx_lt_i32_e32 vcc, 0x102, v134
	v_cmp_le_u32_e64 s[62:63], v24, s76
	v_cmpx_lt_i32_e32 vcc, 0x103, v134
	v_cmp_le_u32_e64 s[64:65], v25, s76
	s_mov_b64 exec, -1
	v_mov_b32_e32 v135, s26
	v_mbcnt_lo_u32_b32 v135, s58, v135
	v_mbcnt_hi_u32_b32 v135, s59, v135
	v_mbcnt_lo_u32_b32 v135, s60, v135
	v_mbcnt_hi_u32_b32 v135, s61, v135
	v_mbcnt_lo_u32_b32 v135, s62, v135
	v_mbcnt_hi_u32_b32 v135, s63, v135
	v_mbcnt_lo_u32_b32 v135, s64, v135
	v_mbcnt_hi_u32_b32 v135, s65, v135
	v_lshlrev_b32_e32 v135, 2, v135
	s_mov_b64 exec, s[58:59]
	v_add_u32_e32 v141, 0x100, v145
	global_store_dword v135, v141, s[40:41]
	v_add_u32_e32 v135, 4, v135
	s_mov_b64 exec, s[60:61]
	v_add_u32_e32 v142, 0x101, v145
	global_store_dword v135, v142, s[40:41]
	v_add_u32_e32 v135, 4, v135
	s_mov_b64 exec, s[62:63]
	v_add_u32_e32 v143, 0x102, v145
	global_store_dword v135, v143, s[40:41]
	v_add_u32_e32 v135, 4, v135
	s_mov_b64 exec, s[64:65]
	v_add_u32_e32 v144, 0x103, v145
	global_store_dword v135, v144, s[40:41]
	v_add_u32_e32 v135, 4, v135
	s_mov_b64 exec, -1
	s_bcnt1_i32_b64 s4, s[58:59]
	s_add_i32 s26, s26, s4
	s_bcnt1_i32_b64 s4, s[60:61]
	s_add_i32 s26, s26, s4
	s_bcnt1_i32_b64 s4, s[62:63]
	s_add_i32 s26, s26, s4
	s_bcnt1_i32_b64 s4, s[64:65]
	s_add_i32 s26, s26, s4
	v_cmpx_lt_i32_e32 vcc, 0x200, v134
	v_cmp_le_u32_e64 s[58:59], v26, s76
	v_cmpx_lt_i32_e32 vcc, 0x201, v134
	v_cmp_le_u32_e64 s[60:61], v27, s76
	v_cmpx_lt_i32_e32 vcc, 0x202, v134
	v_cmp_le_u32_e64 s[62:63], v28, s76
	v_cmpx_lt_i32_e32 vcc, 0x203, v134
	v_cmp_le_u32_e64 s[64:65], v29, s76
	s_mov_b64 exec, -1
	v_mov_b32_e32 v135, s26
	v_mbcnt_lo_u32_b32 v135, s58, v135
	v_mbcnt_hi_u32_b32 v135, s59, v135
	v_mbcnt_lo_u32_b32 v135, s60, v135
	v_mbcnt_hi_u32_b32 v135, s61, v135
	v_mbcnt_lo_u32_b32 v135, s62, v135
	v_mbcnt_hi_u32_b32 v135, s63, v135
	v_mbcnt_lo_u32_b32 v135, s64, v135
	v_mbcnt_hi_u32_b32 v135, s65, v135
	v_lshlrev_b32_e32 v135, 2, v135
	s_mov_b64 exec, s[58:59]
	v_add_u32_e32 v141, 0x200, v145
	global_store_dword v135, v141, s[40:41]
	v_add_u32_e32 v135, 4, v135
	s_mov_b64 exec, s[60:61]
	v_add_u32_e32 v142, 0x201, v145
	global_store_dword v135, v142, s[40:41]
	v_add_u32_e32 v135, 4, v135
	s_mov_b64 exec, s[62:63]
	v_add_u32_e32 v143, 0x202, v145
	global_store_dword v135, v143, s[40:41]
	v_add_u32_e32 v135, 4, v135
	s_mov_b64 exec, s[64:65]
	v_add_u32_e32 v144, 0x203, v145
	global_store_dword v135, v144, s[40:41]
	v_add_u32_e32 v135, 4, v135
	s_mov_b64 exec, -1
	s_bcnt1_i32_b64 s4, s[58:59]
	s_add_i32 s26, s26, s4
	s_bcnt1_i32_b64 s4, s[60:61]
	s_add_i32 s26, s26, s4
	s_bcnt1_i32_b64 s4, s[62:63]
	s_add_i32 s26, s26, s4
	s_bcnt1_i32_b64 s4, s[64:65]
	s_add_i32 s26, s26, s4
	v_cmpx_lt_i32_e32 vcc, 0x300, v134
	v_cmp_le_u32_e64 s[58:59], v30, s76
	v_cmpx_lt_i32_e32 vcc, 0x301, v134
	v_cmp_le_u32_e64 s[60:61], v31, s76
	v_cmpx_lt_i32_e32 vcc, 0x302, v134
	v_cmp_le_u32_e64 s[62:63], v32, s76
	v_cmpx_lt_i32_e32 vcc, 0x303, v134
	v_cmp_le_u32_e64 s[64:65], v33, s76
	s_mov_b64 exec, -1
	v_mov_b32_e32 v135, s26
	v_mbcnt_lo_u32_b32 v135, s58, v135
	v_mbcnt_hi_u32_b32 v135, s59, v135
	v_mbcnt_lo_u32_b32 v135, s60, v135
	v_mbcnt_hi_u32_b32 v135, s61, v135
	v_mbcnt_lo_u32_b32 v135, s62, v135
	v_mbcnt_hi_u32_b32 v135, s63, v135
	v_mbcnt_lo_u32_b32 v135, s64, v135
	v_mbcnt_hi_u32_b32 v135, s65, v135
	v_lshlrev_b32_e32 v135, 2, v135
	s_mov_b64 exec, s[58:59]
	v_add_u32_e32 v141, 0x300, v145
	global_store_dword v135, v141, s[40:41]
	v_add_u32_e32 v135, 4, v135
	s_mov_b64 exec, s[60:61]
	v_add_u32_e32 v142, 0x301, v145
	global_store_dword v135, v142, s[40:41]
	v_add_u32_e32 v135, 4, v135
	s_mov_b64 exec, s[62:63]
	v_add_u32_e32 v143, 0x302, v145
	global_store_dword v135, v143, s[40:41]
	v_add_u32_e32 v135, 4, v135
	s_mov_b64 exec, s[64:65]
	v_add_u32_e32 v144, 0x303, v145
	global_store_dword v135, v144, s[40:41]
	v_add_u32_e32 v135, 4, v135
	s_mov_b64 exec, -1
	s_bcnt1_i32_b64 s4, s[58:59]
	s_add_i32 s26, s26, s4
	s_bcnt1_i32_b64 s4, s[60:61]
	s_add_i32 s26, s26, s4
	s_bcnt1_i32_b64 s4, s[62:63]
	s_add_i32 s26, s26, s4
	s_bcnt1_i32_b64 s4, s[64:65]
	s_add_i32 s26, s26, s4
